# baseline (speedup 1.0000x reference)
.LBB1_13:
	v_mfma_f32_32x32x16_bf16 v[2:17], v[78:81], v[206:209], v[236:251]
	ds_read_b128 v[174:177], v210
	v_add_u32_e32 v195, v230, v228
	v_exp_f32_e32 v199, v28
	v_exp_f32_e32 v198, v32
	v_mfma_f32_32x32x16_bf16 v[2:17], v[74:77], v[190:193], v[2:17]
	ds_read_b128 v[170:173], v210 offset:1024
	v_exp_f32_e32 v197, v20
	v_exp_f32_e32 v196, v24
	v_mfma_f32_32x32x16_bf16 v[2:17], v[70:73], v[158:161], v[2:17]
	ds_read_b128 v[166:169], v210 offset:2048
	v_exp_f32_e32 v18, v18
	v_exp_f32_e32 v22, v22
	v_exp_f32_e32 v24, v26
	v_exp_f32_e32 v26, v30
	v_fma_f32 v20, v197, s12, s12
	v_fma_f32 v28, v196, s12, s12
	v_fma_f32 v30, v199, s12, s12
	v_fma_f32 v32, v198, s12, s12
	v_mfma_f32_32x32x16_bf16 v[2:17], v[66:69], v[142:145], v[2:17]
	ds_read_b128 v[162:165], v210 offset:3072
	v_exp_f32_e32 v19, v19
	v_exp_f32_e32 v23, v23
	v_exp_f32_e32 v27, v27
	v_exp_f32_e32 v31, v31
	v_fmac_f32_e32 v20, v18, v20
	v_fmac_f32_e32 v28, v22, v28
	v_fmac_f32_e32 v30, v24, v30
	v_fmac_f32_e32 v32, v26, v32
	v_mfma_f32_32x32x16_bf16 v[2:17], v[62:65], v[154:157], v[2:17]
	ds_read_b128 v[158:161], v210 offset:4096
	v_add_f32_e32 v22, 1.0, v19
	v_rcp_f32_e32 v19, v20
	v_rcp_f32_e32 v18, v28
	v_add_f32_e32 v20, 1.0, v23
	v_rcp_f32_e32 v191, v30
	v_rcp_f32_e32 v190, v32
	v_mfma_f32_32x32x16_bf16 v[2:17], v[58:61], v[182:185], v[2:17]
	ds_read_b128 v[154:157], v210 offset:5120
	v_exp_f32_e32 v206, v21
	v_exp_f32_e32 v207, v25
	v_add_f32_e32 v23, 1.0, v27
	v_rcp_f32_e32 v192, v20
	v_add_f32_e32 v20, 1.0, v31
	v_rcp_f32_e32 v193, v22
	v_mfma_f32_32x32x16_bf16 v[2:17], v[54:57], v[186:189], v[2:17]
	ds_read_b128 v[142:145], v210 offset:6144
	v_exp_f32_e32 v208, v29
	v_exp_f32_e32 v209, v33
	v_rcp_f32_e32 v183, v23
	v_rcp_f32_e32 v182, v20
	v_mfma_f32_32x32x16_bf16 v[2:17], v[50:53], v[134:137], v[2:17]
	ds_read_b128 v[130:133], v210 offset:7168
	v_fma_f32 v186, -v196, v18, v18
	v_fma_f32 v187, -v197, v19, v19
	ds_read_b128 v[18:21], v231 offset:36928
	ds_read_b128 v[22:25], v231 offset:36944
	ds_read_b128 v[26:29], v231 offset:36960
	ds_read_b128 v[30:33], v231 offset:36976
	v_pk_fma_f32 v[200:201], v[192:193], v[220:221], v[186:187]
	v_pk_fma_f32 v[134:135], v[198:199], v[190:191], v[190:191] neg_lo:[1,0,0] neg_hi:[1,0,0]
	s_nop 0
	v_pk_fma_f32 v[198:199], v[182:183], v[222:223], v[134:135]
	v_mfma_f32_32x32x16_bf16 v[2:17], v[46:49], v[138:141], v[2:17]
	ds_read_b128 v[134:137], v195 offset:16384
	v_add_f32_e32 v182, 1.0, v206
	v_exp_f32_e32 v183, v201
	v_exp_f32_e32 v186, v200
	v_exp_f32_e32 v187, v199
	v_exp_f32_e32 v188, v198
	v_add_f32_e32 v189, 1.0, v207
	v_add_f32_e32 v190, 1.0, v208
	v_add_f32_e32 v191, 1.0, v209
	v_mfma_f32_32x32x16_bf16 v[2:17], v[42:45], v[146:149], v[2:17]
	ds_read_b128 v[138:141], v195 offset:16416
	v_fmac_f32_e32 v182, v182, v183
	v_fmac_f32_e32 v189, v189, v186
	v_fmac_f32_e32 v190, v190, v187
	v_fmac_f32_e32 v191, v191, v188
	v_mfma_f32_32x32x16_bf16 v[2:17], v[38:41], v[150:153], v[2:17]
	ds_read_b128 v[146:149], v195 offset:16448
	v_rcp_f32_e32 v182, v182
	v_rcp_f32_e32 v189, v189
	v_mfma_f32_32x32x16_bf16 v[2:17], v[34:37], v[178:181], v[2:17]
	ds_read_b128 v[150:153], v195 offset:16480
	v_rcp_f32_e32 v190, v190
	v_rcp_f32_e32 v191, v191
	v_fma_f32 v182, -v183, v182, v182
	v_fma_f32 v183, -v186, v189, v189
	s_waitcnt lgkmcnt(4)
	v_mfma_f32_32x32x16_bf16 v[18:33], v[126:129], v[174:177], v[18:33]
	v_fma_f32 v186, -v187, v190, v190
	v_fma_f32 v187, -v188, v191, v191
	v_cvt_pk_bf16_f32 v252, v182, v183
	v_cvt_pk_bf16_f32 v253, v186, v187
	v_mfma_f32_32x32x16_bf16 v[18:33], v[122:125], v[170:173], v[18:33]
	s_nop 1
	v_exp_f32_e32 v179, v4
	v_exp_f32_e32 v178, v8
	v_exp_f32_e32 v181, v12
	v_exp_f32_e32 v180, v16
	v_mfma_f32_32x32x16_bf16 v[18:33], v[118:121], v[166:169], v[18:33]
	v_exp_f32_e32 v2, v2
	v_exp_f32_e32 v6, v6
	v_exp_f32_e32 v10, v10
	v_exp_f32_e32 v12, v14
	v_fma_f32 v4, v179, s12, s12
	v_fma_f32 v8, v178, s12, s12
	v_fma_f32 v14, v181, s12, s12
	v_fma_f32 v16, v180, s12, s12
	v_mfma_f32_32x32x16_bf16 v[18:33], v[114:117], v[162:165], v[18:33]
	v_exp_f32_e32 v3, v3
	v_fmac_f32_e32 v4, v2, v4
	v_exp_f32_e32 v2, v7
	v_fmac_f32_e32 v8, v6, v8
	v_exp_f32_e32 v6, v11
	v_exp_f32_e32 v7, v15
	v_fmac_f32_e32 v14, v10, v14
	v_fmac_f32_e32 v16, v12, v16
	v_mfma_f32_32x32x16_bf16 v[18:33], v[110:113], v[158:161], v[18:33]
	v_add_f32_e32 v10, 1.0, v3
	v_rcp_f32_e32 v3, v4
	v_add_f32_e32 v4, 1.0, v2
	v_rcp_f32_e32 v2, v8
	v_rcp_f32_e32 v183, v14
	v_rcp_f32_e32 v182, v16
	v_mfma_f32_32x32x16_bf16 v[18:33], v[106:109], v[154:157], v[18:33]
	v_add_f32_e32 v6, 1.0, v6
	v_add_f32_e32 v7, 1.0, v7
	v_rcp_f32_e32 v187, v10
	v_rcp_f32_e32 v186, v4
	v_exp_f32_e32 v190, v5
	v_exp_f32_e32 v191, v9
	v_mfma_f32_32x32x16_bf16 v[18:33], v[102:105], v[142:145], v[18:33]
	v_rcp_f32_e32 v189, v6
	v_rcp_f32_e32 v188, v7
	v_exp_f32_e32 v192, v13
	v_exp_f32_e32 v193, v17
	v_mfma_f32_32x32x16_bf16 v[18:33], v[98:101], v[130:133], v[18:33]
	v_fma_f32 v178, -v178, v2, v2
	v_fma_f32 v179, -v179, v3, v3
	v_pk_fma_f32 v[206:207], v[186:187], v[216:217], v[178:179]
	s_nop 0
	v_pk_fma_f32 v[178:179], v[180:181], v[182:183], v[182:183] neg_lo:[1,0,0] neg_hi:[1,0,0]
	s_nop 0
	v_pk_fma_f32 v[208:209], v[188:189], v[218:219], v[178:179]
	s_waitcnt lgkmcnt(0)
	v_mfma_f32_32x32x16_bf16 v[18:33], v[94:97], v[134:137], v[18:33]
	v_add_f32_e32 v178, 1.0, v190
	v_exp_f32_e32 v179, v207
	v_add_f32_e32 v180, 1.0, v191
	v_exp_f32_e32 v181, v206
	v_exp_f32_e32 v182, v209
	v_exp_f32_e32 v183, v208
	v_mfma_f32_32x32x16_bf16 v[18:33], v[90:93], v[138:141], v[18:33]
	v_add_f32_e32 v184, 1.0, v192
	v_add_f32_e32 v185, 1.0, v193
	v_fmac_f32_e32 v178, v178, v179
	v_fmac_f32_e32 v180, v180, v181
	v_fmac_f32_e32 v184, v184, v182
	v_fmac_f32_e32 v185, v185, v183
	v_mfma_f32_32x32x16_bf16 v[18:33], v[86:89], v[146:149], v[18:33]
	v_rcp_f32_e32 v178, v178
	v_rcp_f32_e32 v180, v180
	v_rcp_f32_e32 v184, v184
	v_rcp_f32_e32 v185, v185
	v_mfma_f32_32x32x16_bf16 v[18:33], v[82:85], v[150:153], v[18:33]
	v_fma_f32 v178, -v179, v178, v178
	v_fma_f32 v179, -v181, v180, v180
	v_fma_f32 v180, -v182, v184, v184
	v_fma_f32 v181, -v183, v185, v185
	v_cvt_pk_bf16_f32 v254, v178, v179
	v_cvt_pk_bf16_f32 v255, v180, v181
	ds_write_b128 v211, v[252:255] offset:8192
	s_waitcnt lgkmcnt(0)
	s_barrier
	s_add_i32 s1, s1, 2
	s_cmp_gt_u32 s1, 16
	v_add_u32_e32 v232, 0x200, v232
	s_cbranch_scc1 .LBB1_30
.LBB1_14:
	v_mfma_f32_32x32x16_bf16 v[2:17], v[78:81], v[174:177], v[236:251]
	v_add_u32_e32 v192, v230, v229
	ds_read2_b32 v[228:229], v232 offset1:32
	ds_read_b128 v[194:197], v210 offset:8192
	v_exp_f32_e32 v187, v20
	v_exp_f32_e32 v186, v24
	v_mfma_f32_32x32x16_bf16 v[2:17], v[74:77], v[170:173], v[2:17]
	ds_read_b128 v[178:181], v210 offset:9216
	v_exp_f32_e32 v189, v28
	v_exp_f32_e32 v188, v32
	v_mfma_f32_32x32x16_bf16 v[2:17], v[70:73], v[166:169], v[2:17]
	ds_read_b128 v[170:173], v210 offset:10240
	v_exp_f32_e32 v18, v18
	v_exp_f32_e32 v22, v22
	v_exp_f32_e32 v24, v26
	v_exp_f32_e32 v26, v30
	v_fma_f32 v20, v187, s12, s12
	v_fma_f32 v28, v186, s12, s12
	v_fma_f32 v30, v189, s12, s12
	v_fma_f32 v32, v188, s12, s12
	v_mfma_f32_32x32x16_bf16 v[2:17], v[66:69], v[162:165], v[2:17]
	ds_read_b128 v[166:169], v210 offset:11264
	v_exp_f32_e32 v19, v19
	v_exp_f32_e32 v23, v23
	v_exp_f32_e32 v27, v27
	v_exp_f32_e32 v31, v31
	v_fmac_f32_e32 v20, v18, v20
	v_fmac_f32_e32 v28, v22, v28
	v_fmac_f32_e32 v30, v24, v30
	v_fmac_f32_e32 v32, v26, v32
	v_mfma_f32_32x32x16_bf16 v[2:17], v[62:65], v[158:161], v[2:17]
	ds_read_b128 v[162:165], v210 offset:12288
	v_add_f32_e32 v22, 1.0, v19
	v_rcp_f32_e32 v19, v20
	v_rcp_f32_e32 v18, v28
	v_rcp_f32_e32 v191, v30
	v_rcp_f32_e32 v190, v32
	v_add_f32_e32 v20, 1.0, v23
	v_mfma_f32_32x32x16_bf16 v[2:17], v[58:61], v[154:157], v[2:17]
	ds_read_b128 v[174:177], v210 offset:13312
	v_rcp_f32_e32 v159, v22
	v_rcp_f32_e32 v158, v20
	v_exp_f32_e32 v160, v21
	v_exp_f32_e32 v161, v25
	v_add_f32_e32 v23, 1.0, v27
	v_add_f32_e32 v20, 1.0, v31
	v_mfma_f32_32x32x16_bf16 v[2:17], v[54:57], v[142:145], v[2:17]
	ds_read_b128 v[182:185], v210 offset:14336
	v_rcp_f32_e32 v155, v23
	v_rcp_f32_e32 v154, v20
	v_exp_f32_e32 v193, v29
	v_exp_f32_e32 v217, v33
	v_mfma_f32_32x32x16_bf16 v[2:17], v[50:53], v[130:133], v[2:17]
	ds_read_b128 v[142:145], v210 offset:15360
	v_fma_f32 v156, -v186, v18, v18
	v_fma_f32 v157, -v187, v19, v19
	ds_read_b128 v[18:21], v231 offset:36928
	ds_read_b128 v[22:25], v231 offset:36944
	ds_read_b128 v[26:29], v231 offset:36960
	ds_read_b128 v[30:33], v231 offset:36976
	v_pk_fma_f32 v[214:215], v[158:159], v[214:215], v[156:157]
	v_pk_fma_f32 v[130:131], v[188:189], v[190:191], v[190:191] neg_lo:[1,0,0] neg_hi:[1,0,0]
	s_nop 0
	v_pk_fma_f32 v[212:213], v[154:155], v[212:213], v[130:131]
	v_mfma_f32_32x32x16_bf16 v[2:17], v[46:49], v[134:137], v[2:17]
	ds_read_b128 v[154:157], v192 offset:16384
	v_add_f32_e32 v130, 1.0, v160
	v_exp_f32_e32 v131, v215
	v_exp_f32_e32 v132, v214
	v_exp_f32_e32 v133, v213
	v_exp_f32_e32 v220, v212
	v_add_f32_e32 v134, 1.0, v161
	v_add_f32_e32 v135, 1.0, v193
	v_add_f32_e32 v136, 1.0, v217
	v_mfma_f32_32x32x16_bf16 v[2:17], v[42:45], v[138:141], v[2:17]
	ds_read_b128 v[158:161], v192 offset:16416
	v_fmac_f32_e32 v130, v130, v131
	v_fmac_f32_e32 v134, v134, v132
	v_fmac_f32_e32 v135, v135, v133
	v_fmac_f32_e32 v136, v136, v220
	v_mfma_f32_32x32x16_bf16 v[2:17], v[38:41], v[146:149], v[2:17]
	ds_read_b128 v[186:189], v192 offset:16448
	v_rcp_f32_e32 v130, v130
	v_rcp_f32_e32 v134, v134
	v_mfma_f32_32x32x16_bf16 v[2:17], v[34:37], v[150:153], v[2:17]
	ds_read_b128 v[190:193], v192 offset:16480
	v_rcp_f32_e32 v135, v135
	v_rcp_f32_e32 v136, v136
	v_fma_f32 v130, -v131, v130, v130
	v_fma_f32 v131, -v132, v134, v134
	s_waitcnt lgkmcnt(4)
	v_mfma_f32_32x32x16_bf16 v[18:33], v[126:129], v[194:197], v[18:33]
	v_fma_f32 v132, -v133, v135, v135
	v_fma_f32 v133, -v220, v136, v136
	v_cvt_pk_bf16_f32 v252, v130, v131
	v_cvt_pk_bf16_f32 v253, v132, v133
	v_mfma_f32_32x32x16_bf16 v[18:33], v[122:125], v[178:181], v[18:33]
	s_nop 1
	v_exp_f32_e32 v131, v4
	v_exp_f32_e32 v130, v8
	v_exp_f32_e32 v133, v12
	v_exp_f32_e32 v132, v16
	v_mfma_f32_32x32x16_bf16 v[18:33], v[118:121], v[170:173], v[18:33]
	v_exp_f32_e32 v2, v2
	v_exp_f32_e32 v6, v6
	v_exp_f32_e32 v10, v10
	v_exp_f32_e32 v12, v14
	v_fma_f32 v4, v131, s12, s12
	v_fma_f32 v8, v130, s12, s12
	v_fma_f32 v14, v133, s12, s12
	v_fma_f32 v16, v132, s12, s12
	v_mfma_f32_32x32x16_bf16 v[18:33], v[114:117], v[166:169], v[18:33]
	v_exp_f32_e32 v3, v3
	v_fmac_f32_e32 v4, v2, v4
	v_exp_f32_e32 v2, v7
	v_fmac_f32_e32 v8, v6, v8
	v_exp_f32_e32 v6, v11
	v_exp_f32_e32 v7, v15
	v_fmac_f32_e32 v14, v10, v14
	v_fmac_f32_e32 v16, v12, v16
	v_mfma_f32_32x32x16_bf16 v[18:33], v[110:113], v[162:165], v[18:33]
	v_add_f32_e32 v10, 1.0, v3
	v_rcp_f32_e32 v3, v4
	v_add_f32_e32 v4, 1.0, v2
	v_rcp_f32_e32 v2, v8
	v_rcp_f32_e32 v135, v14
	v_rcp_f32_e32 v134, v16
	v_mfma_f32_32x32x16_bf16 v[18:33], v[106:109], v[174:177], v[18:33]
	v_add_f32_e32 v6, 1.0, v6
	v_add_f32_e32 v7, 1.0, v7
	v_rcp_f32_e32 v137, v10
	v_rcp_f32_e32 v136, v4
	v_exp_f32_e32 v140, v5
	v_exp_f32_e32 v141, v9
	v_mfma_f32_32x32x16_bf16 v[18:33], v[102:105], v[182:185], v[18:33]
	v_rcp_f32_e32 v139, v6
	v_rcp_f32_e32 v138, v7
	v_exp_f32_e32 v146, v13
	v_exp_f32_e32 v147, v17
	v_mfma_f32_32x32x16_bf16 v[18:33], v[98:101], v[142:145], v[18:33]
	v_fma_f32 v130, -v130, v2, v2
	v_fma_f32 v131, -v131, v3, v3
	v_pk_fma_f32 v[224:225], v[136:137], v[204:205], v[130:131]
	s_nop 0
	v_pk_fma_f32 v[130:131], v[132:133], v[134:135], v[134:135] neg_lo:[1,0,0] neg_hi:[1,0,0]
	s_nop 0
	v_pk_fma_f32 v[226:227], v[138:139], v[202:203], v[130:131]
	s_waitcnt lgkmcnt(0)
	v_mfma_f32_32x32x16_bf16 v[18:33], v[94:97], v[154:157], v[18:33]
	v_add_f32_e32 v130, 1.0, v140
	v_exp_f32_e32 v131, v225
	v_add_f32_e32 v132, 1.0, v141
	v_exp_f32_e32 v133, v224
	v_exp_f32_e32 v134, v227
	v_exp_f32_e32 v135, v226
	v_mfma_f32_32x32x16_bf16 v[18:33], v[90:93], v[158:161], v[18:33]
	v_add_f32_e32 v136, 1.0, v146
	v_add_f32_e32 v137, 1.0, v147
	v_fmac_f32_e32 v130, v130, v131
	v_fmac_f32_e32 v132, v132, v133
	v_fmac_f32_e32 v136, v136, v134
	v_fmac_f32_e32 v137, v137, v135
	v_mfma_f32_32x32x16_bf16 v[18:33], v[86:89], v[186:189], v[18:33]
	v_rcp_f32_e32 v130, v130
	v_rcp_f32_e32 v132, v132
	v_rcp_f32_e32 v136, v136
	v_rcp_f32_e32 v137, v137
	v_mfma_f32_32x32x16_bf16 v[18:33], v[82:85], v[190:193], v[18:33]
	v_fma_f32 v130, -v131, v130, v130
	v_fma_f32 v131, -v133, v132, v132
	v_fma_f32 v132, -v134, v136, v136
	v_fma_f32 v133, -v135, v137, v137
	v_cvt_pk_bf16_f32 v254, v130, v131
	v_cvt_pk_bf16_f32 v255, v132, v133
	ds_write_b128 v211, v[252:255] offset:0
	s_waitcnt lgkmcnt(0)
	s_barrier
	v_mfma_f32_32x32x16_bf16 v[2:17], v[78:81], v[194:197], v[236:251]
	ds_read_b128 v[202:205], v210
	v_add_u32_e32 v216, v230, v228
	v_exp_f32_e32 v147, v20
	v_exp_f32_e32 v146, v24
	v_mfma_f32_32x32x16_bf16 v[2:17], v[74:77], v[178:181], v[2:17]
	ds_read_b128 v[194:197], v210 offset:1024
	v_exp_f32_e32 v149, v28
	v_exp_f32_e32 v148, v32
	v_mfma_f32_32x32x16_bf16 v[2:17], v[70:73], v[170:173], v[2:17]
	ds_read_b128 v[138:141], v210 offset:2048
	v_exp_f32_e32 v18, v18
	v_exp_f32_e32 v22, v22
	v_exp_f32_e32 v24, v26
	v_exp_f32_e32 v26, v30
	v_fma_f32 v20, v147, s12, s12
	v_fma_f32 v28, v146, s12, s12
	v_fma_f32 v30, v149, s12, s12
	v_fma_f32 v32, v148, s12, s12
	v_mfma_f32_32x32x16_bf16 v[2:17], v[66:69], v[166:169], v[2:17]
	ds_read_b128 v[134:137], v210 offset:3072
	v_exp_f32_e32 v19, v19
	v_exp_f32_e32 v23, v23
	v_exp_f32_e32 v27, v27
	v_exp_f32_e32 v31, v31
	v_fmac_f32_e32 v20, v18, v20
	v_fmac_f32_e32 v28, v22, v28
	v_fmac_f32_e32 v30, v24, v30
	v_fmac_f32_e32 v32, v26, v32
	v_mfma_f32_32x32x16_bf16 v[2:17], v[62:65], v[162:165], v[2:17]
	ds_read_b128 v[166:169], v210 offset:4096
	v_add_f32_e32 v22, 1.0, v19
	v_rcp_f32_e32 v19, v20
	v_rcp_f32_e32 v18, v28
	v_rcp_f32_e32 v151, v30
	v_rcp_f32_e32 v150, v32
	v_add_f32_e32 v20, 1.0, v23
	v_mfma_f32_32x32x16_bf16 v[2:17], v[58:61], v[174:177], v[2:17]
	ds_read_b128 v[162:165], v210 offset:5120
	v_rcp_f32_e32 v153, v22
	v_rcp_f32_e32 v152, v20
	v_add_f32_e32 v23, 1.0, v27
	v_add_f32_e32 v20, 1.0, v31
	v_exp_f32_e32 v180, v21
	v_exp_f32_e32 v181, v25
	v_mfma_f32_32x32x16_bf16 v[2:17], v[54:57], v[182:185], v[2:17]
	ds_read_b128 v[170:173], v210 offset:6144
	v_rcp_f32_e32 v175, v23
	v_rcp_f32_e32 v174, v20
	v_exp_f32_e32 v176, v29
	v_exp_f32_e32 v177, v33
	v_mfma_f32_32x32x16_bf16 v[2:17], v[50:53], v[142:145], v[2:17]
	ds_read_b128 v[130:133], v210 offset:7168
	v_fma_f32 v146, -v146, v18, v18
	v_fma_f32 v147, -v147, v19, v19
	ds_read_b128 v[18:21], v231 offset:36928
	ds_read_b128 v[22:25], v231 offset:36944
	ds_read_b128 v[26:29], v231 offset:36960
	ds_read_b128 v[30:33], v231 offset:36976
	v_pk_fma_f32 v[220:221], v[152:153], v[200:201], v[146:147]
	v_pk_fma_f32 v[142:143], v[148:149], v[150:151], v[150:151] neg_lo:[1,0,0] neg_hi:[1,0,0]
	s_nop 0
	v_pk_fma_f32 v[222:223], v[174:175], v[198:199], v[142:143]
	v_mfma_f32_32x32x16_bf16 v[2:17], v[46:49], v[154:157], v[2:17]
	ds_read_b128 v[146:149], v216 offset:16384
	v_add_f32_e32 v142, 1.0, v180
	v_exp_f32_e32 v143, v221
	v_exp_f32_e32 v144, v220
	v_exp_f32_e32 v145, v223
	v_exp_f32_e32 v180, v222
	v_add_f32_e32 v154, 1.0, v181
	v_add_f32_e32 v155, 1.0, v176
	v_add_f32_e32 v156, 1.0, v177
	v_mfma_f32_32x32x16_bf16 v[2:17], v[42:45], v[158:161], v[2:17]
	ds_read_b128 v[150:153], v216 offset:16416
	v_fmac_f32_e32 v142, v142, v143
	v_fmac_f32_e32 v154, v154, v144
	v_fmac_f32_e32 v155, v155, v145
	v_fmac_f32_e32 v156, v156, v180
	v_mfma_f32_32x32x16_bf16 v[2:17], v[38:41], v[186:189], v[2:17]
	ds_read_b128 v[174:177], v216 offset:16448
	v_rcp_f32_e32 v142, v142
	v_rcp_f32_e32 v154, v154
	v_mfma_f32_32x32x16_bf16 v[2:17], v[34:37], v[190:193], v[2:17]
	ds_read_b128 v[198:201], v216 offset:16480
	v_rcp_f32_e32 v155, v155
	v_rcp_f32_e32 v156, v156
	v_fma_f32 v142, -v143, v142, v142
	v_fma_f32 v143, -v144, v154, v154
	s_waitcnt lgkmcnt(4)
	v_mfma_f32_32x32x16_bf16 v[18:33], v[126:129], v[202:205], v[18:33]
	v_fma_f32 v144, -v145, v155, v155
	v_fma_f32 v145, -v180, v156, v156
	v_cvt_pk_bf16_f32 v252, v142, v143
	v_cvt_pk_bf16_f32 v253, v144, v145
	v_mfma_f32_32x32x16_bf16 v[18:33], v[122:125], v[194:197], v[18:33]
	s_nop 1
	v_exp_f32_e32 v143, v4
	v_exp_f32_e32 v142, v8
	v_exp_f32_e32 v145, v12
	v_exp_f32_e32 v144, v16
	v_mfma_f32_32x32x16_bf16 v[18:33], v[118:121], v[138:141], v[18:33]
	v_exp_f32_e32 v2, v2
	v_exp_f32_e32 v6, v6
	v_exp_f32_e32 v10, v10
	v_exp_f32_e32 v12, v14
	v_fma_f32 v4, v143, s12, s12
	v_fma_f32 v8, v142, s12, s12
	v_fma_f32 v14, v145, s12, s12
	v_fma_f32 v16, v144, s12, s12
	v_mfma_f32_32x32x16_bf16 v[18:33], v[114:117], v[134:137], v[18:33]
	v_exp_f32_e32 v3, v3
	v_fmac_f32_e32 v4, v2, v4
	v_exp_f32_e32 v2, v7
	v_fmac_f32_e32 v8, v6, v8
	v_exp_f32_e32 v6, v11
	v_exp_f32_e32 v7, v15
	v_fmac_f32_e32 v14, v10, v14
	v_fmac_f32_e32 v16, v12, v16
	v_mfma_f32_32x32x16_bf16 v[18:33], v[110:113], v[166:169], v[18:33]
	v_add_f32_e32 v10, 1.0, v3
	v_rcp_f32_e32 v3, v4
	v_add_f32_e32 v4, 1.0, v2
	v_rcp_f32_e32 v2, v8
	v_rcp_f32_e32 v155, v14
	v_rcp_f32_e32 v154, v16
	v_mfma_f32_32x32x16_bf16 v[18:33], v[106:109], v[162:165], v[18:33]
	v_add_f32_e32 v6, 1.0, v6
	v_add_f32_e32 v7, 1.0, v7
	v_rcp_f32_e32 v157, v10
	v_rcp_f32_e32 v156, v4
	v_exp_f32_e32 v160, v5
	v_exp_f32_e32 v161, v9
	v_mfma_f32_32x32x16_bf16 v[18:33], v[102:105], v[170:173], v[18:33]
	v_rcp_f32_e32 v159, v6
	v_rcp_f32_e32 v158, v7
	v_exp_f32_e32 v180, v13
	v_exp_f32_e32 v181, v17
	v_mfma_f32_32x32x16_bf16 v[18:33], v[98:101], v[130:133], v[18:33]
	v_fma_f32 v142, -v142, v2, v2
	v_fma_f32 v143, -v143, v3, v3
	v_pk_fma_f32 v[216:217], v[156:157], v[206:207], v[142:143]
	s_nop 0
	v_pk_fma_f32 v[142:143], v[144:145], v[154:155], v[154:155] neg_lo:[1,0,0] neg_hi:[1,0,0]
	s_nop 0
	v_pk_fma_f32 v[218:219], v[158:159], v[208:209], v[142:143]
	s_waitcnt lgkmcnt(0)
	v_mfma_f32_32x32x16_bf16 v[18:33], v[94:97], v[146:149], v[18:33]
	v_add_f32_e32 v142, 1.0, v160
	v_exp_f32_e32 v143, v217
	v_add_f32_e32 v144, 1.0, v161
	v_exp_f32_e32 v145, v216
	v_exp_f32_e32 v154, v219
	v_exp_f32_e32 v155, v218
	v_mfma_f32_32x32x16_bf16 v[18:33], v[90:93], v[150:153], v[18:33]
	v_add_f32_e32 v156, 1.0, v180
	v_add_f32_e32 v157, 1.0, v181
	v_fmac_f32_e32 v142, v142, v143
	v_fmac_f32_e32 v144, v144, v145
	v_fmac_f32_e32 v156, v156, v154
	v_fmac_f32_e32 v157, v157, v155
	v_mfma_f32_32x32x16_bf16 v[18:33], v[86:89], v[174:177], v[18:33]
	v_rcp_f32_e32 v142, v142
	v_rcp_f32_e32 v144, v144
	v_rcp_f32_e32 v156, v156
	v_rcp_f32_e32 v157, v157
	v_mfma_f32_32x32x16_bf16 v[18:33], v[82:85], v[198:201], v[18:33]
	v_fma_f32 v142, -v143, v142, v142
	v_fma_f32 v143, -v145, v144, v144
	v_fma_f32 v144, -v154, v156, v156
	v_fma_f32 v145, -v155, v157, v157
	v_cvt_pk_bf16_f32 v254, v142, v143
	v_cvt_pk_bf16_f32 v255, v144, v145
	ds_write_b128 v211, v[252:255] offset:8192
	s_waitcnt lgkmcnt(0)
	s_barrier
	v_mfma_f32_32x32x16_bf16 v[2:17], v[78:81], v[202:205], v[236:251]
	v_add_u32_e32 v234, v230, v229
	ds_read2_b32 v[228:229], v232 offset0:64 offset1:96
	ds_read_b128 v[206:209], v210 offset:8192
	v_exp_f32_e32 v179, v20
	v_exp_f32_e32 v178, v24
	v_mfma_f32_32x32x16_bf16 v[2:17], v[74:77], v[194:197], v[2:17]
	ds_read_b128 v[190:193], v210 offset:9216
	v_exp_f32_e32 v181, v28
	v_exp_f32_e32 v180, v32
	v_mfma_f32_32x32x16_bf16 v[2:17], v[70:73], v[138:141], v[2:17]
	ds_read_b128 v[158:161], v210 offset:10240
	v_exp_f32_e32 v18, v18
	v_exp_f32_e32 v22, v22
	v_exp_f32_e32 v24, v26
	v_exp_f32_e32 v26, v30
	v_fma_f32 v20, v179, s12, s12
	v_fma_f32 v28, v178, s12, s12
	v_fma_f32 v30, v181, s12, s12
	v_fma_f32 v32, v180, s12, s12
	v_mfma_f32_32x32x16_bf16 v[2:17], v[66:69], v[134:137], v[2:17]
	ds_read_b128 v[142:145], v210 offset:11264
	v_exp_f32_e32 v19, v19
	v_exp_f32_e32 v23, v23
	v_exp_f32_e32 v27, v27
	v_exp_f32_e32 v31, v31
	v_fmac_f32_e32 v20, v18, v20
	v_fmac_f32_e32 v28, v22, v28
	v_fmac_f32_e32 v30, v24, v30
	v_fmac_f32_e32 v32, v26, v32
	v_mfma_f32_32x32x16_bf16 v[2:17], v[62:65], v[166:169], v[2:17]
	ds_read_b128 v[154:157], v210 offset:12288
	v_add_f32_e32 v22, 1.0, v19
	v_rcp_f32_e32 v19, v20
	v_rcp_f32_e32 v18, v28
	v_rcp_f32_e32 v139, v30
	v_rcp_f32_e32 v138, v32
	v_add_f32_e32 v20, 1.0, v23
	v_mfma_f32_32x32x16_bf16 v[2:17], v[58:61], v[162:165], v[2:17]
	ds_read_b128 v[182:185], v210 offset:13312
	v_rcp_f32_e32 v141, v22
	v_rcp_f32_e32 v140, v20
	v_add_f32_e32 v23, 1.0, v27
	v_add_f32_e32 v20, 1.0, v31
	v_exp_f32_e32 v168, v21
	v_exp_f32_e32 v169, v25
	v_mfma_f32_32x32x16_bf16 v[2:17], v[54:57], v[170:173], v[2:17]
	ds_read_b128 v[186:189], v210 offset:14336
	v_rcp_f32_e32 v163, v23
	v_rcp_f32_e32 v162, v20
	v_exp_f32_e32 v194, v29
	v_exp_f32_e32 v195, v33
	v_mfma_f32_32x32x16_bf16 v[2:17], v[50:53], v[130:133], v[2:17]
	ds_read_b128 v[134:137], v210 offset:15360
	v_fma_f32 v166, -v178, v18, v18
	v_fma_f32 v167, -v179, v19, v19
	ds_read_b128 v[18:21], v231 offset:36928
	ds_read_b128 v[22:25], v231 offset:36944
	ds_read_b128 v[26:29], v231 offset:36960
	ds_read_b128 v[30:33], v231 offset:36976
	v_pk_fma_f32 v[214:215], v[140:141], v[214:215], v[166:167]
	v_pk_fma_f32 v[130:131], v[180:181], v[138:139], v[138:139] neg_lo:[1,0,0] neg_hi:[1,0,0]
	s_nop 0
	v_pk_fma_f32 v[212:213], v[162:163], v[212:213], v[130:131]
	v_mfma_f32_32x32x16_bf16 v[2:17], v[46:49], v[146:149], v[2:17]
	ds_read_b128 v[138:141], v234 offset:16384
	v_add_f32_e32 v130, 1.0, v168
	v_exp_f32_e32 v131, v215
	v_exp_f32_e32 v132, v214
	v_exp_f32_e32 v133, v213
	v_exp_f32_e32 v162, v212
	v_add_f32_e32 v163, 1.0, v169
	v_add_f32_e32 v166, 1.0, v194
	v_add_f32_e32 v167, 1.0, v195
	v_mfma_f32_32x32x16_bf16 v[2:17], v[42:45], v[150:153], v[2:17]
	ds_read_b128 v[146:149], v234 offset:16416
	v_fmac_f32_e32 v130, v130, v131
	v_fmac_f32_e32 v163, v163, v132
	v_fmac_f32_e32 v166, v166, v133
	v_fmac_f32_e32 v167, v167, v162
	v_mfma_f32_32x32x16_bf16 v[2:17], v[38:41], v[174:177], v[2:17]
	ds_read_b128 v[150:153], v234 offset:16448
	v_rcp_f32_e32 v130, v130
	v_rcp_f32_e32 v163, v163
	v_mfma_f32_32x32x16_bf16 v[2:17], v[34:37], v[198:201], v[2:17]
	ds_read_b128 v[178:181], v234 offset:16480
	v_rcp_f32_e32 v166, v166
	v_rcp_f32_e32 v167, v167
	v_fma_f32 v130, -v131, v130, v130
	v_fma_f32 v131, -v132, v163, v163
	s_waitcnt lgkmcnt(4)
	v_mfma_f32_32x32x16_bf16 v[18:33], v[126:129], v[206:209], v[18:33]
	v_fma_f32 v132, -v133, v166, v166
	v_fma_f32 v133, -v162, v167, v167
	v_cvt_pk_bf16_f32 v252, v130, v131
	v_cvt_pk_bf16_f32 v253, v132, v133
	v_mfma_f32_32x32x16_bf16 v[18:33], v[122:125], v[190:193], v[18:33]
	s_nop 1
	v_exp_f32_e32 v131, v4
	v_exp_f32_e32 v130, v8
	v_exp_f32_e32 v133, v12
	v_exp_f32_e32 v132, v16
	v_mfma_f32_32x32x16_bf16 v[18:33], v[118:121], v[158:161], v[18:33]
	v_exp_f32_e32 v2, v2
	v_exp_f32_e32 v6, v6
	v_exp_f32_e32 v10, v10
	v_exp_f32_e32 v12, v14
	v_fma_f32 v4, v131, s12, s12
	v_fma_f32 v8, v130, s12, s12
	v_fma_f32 v14, v133, s12, s12
	v_fma_f32 v16, v132, s12, s12
	v_mfma_f32_32x32x16_bf16 v[18:33], v[114:117], v[142:145], v[18:33]
	v_exp_f32_e32 v3, v3
	v_fmac_f32_e32 v4, v2, v4
	v_exp_f32_e32 v2, v7
	v_fmac_f32_e32 v8, v6, v8
	v_exp_f32_e32 v6, v11
	v_exp_f32_e32 v7, v15
	v_fmac_f32_e32 v14, v10, v14
	v_fmac_f32_e32 v16, v12, v16
	v_mfma_f32_32x32x16_bf16 v[18:33], v[110:113], v[154:157], v[18:33]
	v_add_f32_e32 v10, 1.0, v3
	v_rcp_f32_e32 v3, v4
	v_add_f32_e32 v4, 1.0, v2
	v_rcp_f32_e32 v2, v8
	v_rcp_f32_e32 v163, v14
	v_rcp_f32_e32 v162, v16
	v_mfma_f32_32x32x16_bf16 v[18:33], v[106:109], v[182:185], v[18:33]
	v_add_f32_e32 v6, 1.0, v6
	v_add_f32_e32 v7, 1.0, v7
	v_rcp_f32_e32 v167, v10
	v_rcp_f32_e32 v166, v4
	v_exp_f32_e32 v170, v5
	v_exp_f32_e32 v171, v9
	v_mfma_f32_32x32x16_bf16 v[18:33], v[102:105], v[186:189], v[18:33]
	v_rcp_f32_e32 v169, v6
	v_rcp_f32_e32 v168, v7
	v_exp_f32_e32 v172, v13
	v_exp_f32_e32 v173, v17
	v_mfma_f32_32x32x16_bf16 v[18:33], v[98:101], v[134:137], v[18:33]
	v_fma_f32 v130, -v130, v2, v2
	v_fma_f32 v131, -v131, v3, v3
	v_pk_fma_f32 v[204:205], v[166:167], v[224:225], v[130:131]
	s_nop 0
	v_pk_fma_f32 v[130:131], v[132:133], v[162:163], v[162:163] neg_lo:[1,0,0] neg_hi:[1,0,0]
	s_nop 0
	v_pk_fma_f32 v[202:203], v[168:169], v[226:227], v[130:131]
	s_waitcnt lgkmcnt(0)
	v_mfma_f32_32x32x16_bf16 v[18:33], v[94:97], v[138:141], v[18:33]
	v_add_f32_e32 v130, 1.0, v170
	v_exp_f32_e32 v131, v205
	v_add_f32_e32 v132, 1.0, v171
	v_exp_f32_e32 v133, v204
	v_exp_f32_e32 v162, v203
	v_exp_f32_e32 v163, v202
	v_mfma_f32_32x32x16_bf16 v[18:33], v[90:93], v[146:149], v[18:33]
	v_add_f32_e32 v164, 1.0, v172
	v_add_f32_e32 v165, 1.0, v173
	v_fmac_f32_e32 v130, v130, v131
	v_fmac_f32_e32 v132, v132, v133
	v_fmac_f32_e32 v164, v164, v162
	v_fmac_f32_e32 v165, v165, v163
	v_mfma_f32_32x32x16_bf16 v[18:33], v[86:89], v[150:153], v[18:33]
	v_rcp_f32_e32 v130, v130
	v_rcp_f32_e32 v132, v132
	v_rcp_f32_e32 v164, v164
	v_rcp_f32_e32 v165, v165
	v_mfma_f32_32x32x16_bf16 v[18:33], v[82:85], v[178:181], v[18:33]
	v_fma_f32 v130, -v131, v130, v130
	v_fma_f32 v131, -v133, v132, v132
	v_fma_f32 v132, -v162, v164, v164
	v_fma_f32 v133, -v163, v165, v165
	v_cvt_pk_bf16_f32 v254, v130, v131
	v_cvt_pk_bf16_f32 v255, v132, v133
	ds_write_b128 v211, v[252:255] offset:0
	s_waitcnt lgkmcnt(0)
	s_barrier
	s_branch .LBB1_13
